# v10 + grid barrier: released workgroups watch the cross-XCC generation word directly (no relay through the XCC leader)
# speedup vs baseline: 1.0077x; 1.0045x over previous
.LBB0_2787:
	s_or_b64 exec, exec, s[6:7]
	v_cvt_f32_u32_e32 v5, v3
	s_waitcnt vmcnt(0)
	v_readfirstlane_b32 s4, v4
	v_sub_u32_e32 v4, 0, v3
	v_rcp_iflag_f32_e32 v5, v5
	v_add_u32_e32 v6, s4, v2
	v_mul_f32_e32 v5, 0x4f7ffffe, v5
	v_cvt_u32_f32_e32 v5, v5
	v_mul_lo_u32 v2, v4, v5
	v_mul_hi_u32 v2, v5, v2
	v_add_u32_e32 v2, v5, v2
	v_mul_hi_u32 v2, v6, v2
	v_mul_lo_u32 v4, v2, v3
	v_sub_u32_e32 v4, v6, v4
	v_add_u32_e32 v5, 1, v2
	v_cmp_ge_u32_e32 vcc, v4, v3
	s_nop 1
	v_cndmask_b32_e32 v2, v2, v5, vcc
	v_sub_u32_e32 v5, v4, v3
	v_cndmask_b32_e32 v4, v4, v5, vcc
	v_add_u32_e32 v5, 1, v2
	v_cmp_ge_u32_e32 vcc, v4, v3
	v_add_u32_e32 v4, 1, v6
	s_nop 0
	v_cndmask_b32_e32 v2, v2, v5, vcc
	v_mul_lo_u32 v5, v3, v2
	v_add_u32_e32 v3, v5, v3
	v_cmp_ne_u32_e32 vcc, v4, v3
	s_and_saveexec_b64 s[4:5], vcc
	s_xor_b64 s[4:5], exec, s[4:5]
	s_cbranch_execz .LBB0_2801
	s_waitcnt lgkmcnt(0)
	v_mov_b32_e32 v1, 0x3100
	global_load_dword v1, v1, s[18:19] offset:1024 sc1
	s_add_u32 s8, s18, 0x3500
	s_addc_u32 s9, s19, 0
	s_waitcnt vmcnt(0)
	v_cmp_eq_u32_e32 vcc, v1, v2
	s_and_saveexec_b64 s[6:7], vcc
	s_cbranch_execz .LBB0_2800
	s_mov_b32 s24, 1
	s_mov_b64 s[10:11], 0
	v_mov_b32_e32 v1, 0
	s_branch .LBB0_2791

.LBB0_2883:
	s_or_b64 exec, exec, s[4:5]
	v_cvt_f32_u32_e32 v6, v4
	s_waitcnt vmcnt(0)
	v_readfirstlane_b32 s3, v5
	v_sub_u32_e32 v5, 0, v4
	v_rcp_iflag_f32_e32 v6, v6
	v_add_u32_e32 v7, s3, v1
	v_mul_f32_e32 v6, 0x4f7ffffe, v6
	v_cvt_u32_f32_e32 v6, v6
	v_mul_lo_u32 v1, v5, v6
	v_mul_hi_u32 v1, v6, v1
	v_add_u32_e32 v1, v6, v1
	v_mul_hi_u32 v1, v7, v1
	v_mul_lo_u32 v5, v1, v4
	v_sub_u32_e32 v5, v7, v5
	v_add_u32_e32 v6, 1, v1
	v_cmp_ge_u32_e32 vcc, v5, v4
	s_nop 1
	v_cndmask_b32_e32 v1, v1, v6, vcc
	v_sub_u32_e32 v6, v5, v4
	v_cndmask_b32_e32 v5, v5, v6, vcc
	v_add_u32_e32 v6, 1, v1
	v_cmp_ge_u32_e32 vcc, v5, v4
	v_add_u32_e32 v5, 1, v7
	s_nop 0
	v_cndmask_b32_e32 v1, v1, v6, vcc
	v_mul_lo_u32 v6, v4, v1
	v_add_u32_e32 v4, v6, v4
	v_cmp_ne_u32_e32 vcc, v5, v4
	s_and_saveexec_b64 s[4:5], vcc
	s_xor_b64 s[4:5], exec, s[4:5]
	s_cbranch_execz .LBB0_2897
	v_readlane_b32 s8, v252, 47
	v_readlane_b32 s9, v252, 48
	s_waitcnt lgkmcnt(0)
	s_nop 3
	global_load_dword v2, v3, s[8:9] sc1
	s_waitcnt vmcnt(0)
	v_cmp_eq_u32_e32 vcc, v2, v1
	s_and_saveexec_b64 s[20:21], vcc
	s_cbranch_execz .LBB0_2896
	s_mov_b32 s3, 1
	s_mov_b64 s[24:25], 0
	s_branch .LBB0_2887

.LBB0_7092:
	s_or_b64 exec, exec, s[4:5]
	v_cvt_f32_u32_e32 v6, v4
	s_waitcnt vmcnt(0)
	v_readfirstlane_b32 s2, v5
	v_sub_u32_e32 v5, 0, v4
	v_rcp_iflag_f32_e32 v6, v6
	v_add_u32_e32 v7, s2, v1
	v_mul_f32_e32 v6, 0x4f7ffffe, v6
	v_cvt_u32_f32_e32 v6, v6
	v_mul_lo_u32 v1, v5, v6
	v_mul_hi_u32 v1, v6, v1
	v_add_u32_e32 v1, v6, v1
	v_mul_hi_u32 v1, v7, v1
	v_mul_lo_u32 v5, v1, v4
	v_sub_u32_e32 v5, v7, v5
	v_add_u32_e32 v6, 1, v1
	v_cmp_ge_u32_e32 vcc, v5, v4
	s_nop 1
	v_cndmask_b32_e32 v1, v1, v6, vcc
	v_sub_u32_e32 v6, v5, v4
	v_cndmask_b32_e32 v5, v5, v6, vcc
	v_add_u32_e32 v6, 1, v1
	v_cmp_ge_u32_e32 vcc, v5, v4
	v_add_u32_e32 v5, 1, v7
	s_nop 0
	v_cndmask_b32_e32 v1, v1, v6, vcc
	v_mul_lo_u32 v6, v4, v1
	v_add_u32_e32 v4, v6, v4
	v_cmp_ne_u32_e32 vcc, v5, v4
	s_and_saveexec_b64 s[2:3], vcc
	s_xor_b64 s[4:5], exec, s[2:3]
	s_cbranch_execz .LBB0_7106
	v_readlane_b32 s2, v252, 47
	v_readlane_b32 s3, v252, 48
	s_waitcnt lgkmcnt(0)
	s_nop 3
	global_load_dword v2, v3, s[2:3] sc1
	s_waitcnt vmcnt(0)
	v_cmp_eq_u32_e32 vcc, v2, v1
	s_and_saveexec_b64 s[20:21], vcc
	s_cbranch_execz .LBB0_7105
	s_mov_b32 s2, 1
	s_mov_b64 s[24:25], 0
	s_branch .LBB0_7096

.LBB0_10853:
	s_or_b64 exec, exec, s[4:5]
	v_cvt_f32_u32_e32 v6, v4
	s_waitcnt vmcnt(0)
	v_readfirstlane_b32 s2, v5
	v_sub_u32_e32 v5, 0, v4
	v_rcp_iflag_f32_e32 v6, v6
	v_add_u32_e32 v7, s2, v1
	v_mul_f32_e32 v6, 0x4f7ffffe, v6
	v_cvt_u32_f32_e32 v6, v6
	v_mul_lo_u32 v1, v5, v6
	v_mul_hi_u32 v1, v6, v1
	v_add_u32_e32 v1, v6, v1
	v_mul_hi_u32 v1, v7, v1
	v_mul_lo_u32 v5, v1, v4
	v_sub_u32_e32 v5, v7, v5
	v_add_u32_e32 v6, 1, v1
	v_cmp_ge_u32_e32 vcc, v5, v4
	s_nop 1
	v_cndmask_b32_e32 v1, v1, v6, vcc
	v_sub_u32_e32 v6, v5, v4
	v_cndmask_b32_e32 v5, v5, v6, vcc
	v_add_u32_e32 v6, 1, v1
	v_cmp_ge_u32_e32 vcc, v5, v4
	v_add_u32_e32 v5, 1, v7
	s_nop 0
	v_cndmask_b32_e32 v1, v1, v6, vcc
	v_mul_lo_u32 v6, v4, v1
	v_add_u32_e32 v4, v6, v4
	v_cmp_ne_u32_e32 vcc, v5, v4
	s_and_saveexec_b64 s[2:3], vcc
	s_xor_b64 s[4:5], exec, s[2:3]
	s_cbranch_execz .LBB0_10867
	v_readlane_b32 s2, v252, 47
	v_readlane_b32 s3, v252, 48
	s_waitcnt lgkmcnt(0)
	s_nop 3
	global_load_dword v2, v3, s[2:3] sc1
	s_waitcnt vmcnt(0)
	v_cmp_eq_u32_e32 vcc, v2, v1
	s_and_saveexec_b64 s[8:9], vcc
	s_cbranch_execz .LBB0_10866
	s_mov_b32 s2, 1
	s_mov_b64 s[20:21], 0
	s_branch .LBB0_10857
